# attention softmax: speculative fast path (exps+sums, test partial row sum <= 2^11.5) without the row-max tree; rare path recomputes QK and does the exact max-based update; on top of v29
# speedup vs baseline: 1.0048x; 1.0006x over previous
.LBB0_809:
	s_nop 9
	v_exp_f32_e32 v82, v82
	v_exp_f32_e32 v66, v66
	v_exp_f32_e32 v175, v83
	v_exp_f32_e32 v67, v67
	v_exp_f32_e32 v84, v84
	v_exp_f32_e32 v68, v68
	v_exp_f32_e32 v85, v85
	v_exp_f32_e32 v69, v69
	v_add_f32_e32 v83, v66, v82
	v_exp_f32_e32 v86, v86
	v_exp_f32_e32 v70, v70
	v_add_f32_e32 v83, 0, v83
	v_add_f32_e32 v176, v67, v175
	v_add_f32_e32 v83, v176, v83
	v_add_f32_e32 v176, v68, v84
	v_add_f32_e32 v83, v176, v83
	v_add_f32_e32 v176, v69, v85
	v_add_f32_e32 v83, v176, v83
	v_add_f32_e32 v176, v70, v86
	v_exp_f32_e32 v87, v87
	v_exp_f32_e32 v71, v71
	v_add_f32_e32 v178, v176, v83
	v_exp_f32_e32 v88, v88
	v_exp_f32_e32 v72, v72
	v_add_f32_e32 v179, v71, v87
	v_exp_f32_e32 v176, v89
	v_exp_f32_e32 v83, v73
	v_add_f32_e32 v73, v179, v178
	v_add_f32_e32 v89, v72, v88
	v_add_f32_e32 v178, v89, v73
	v_exp_f32_e32 v89, v90
	v_exp_f32_e32 v73, v74
	v_add_f32_e32 v179, v83, v176
	v_exp_f32_e32 v90, v91
	v_mov_b32_e32 v74, v75
	v_add_f32_e32 v75, v179, v178
	v_add_f32_e32 v91, v73, v89
	v_add_f32_e32 v178, v91, v75
	v_exp_f32_e32 v74, v74
	v_exp_f32_e32 v91, v92
	v_exp_f32_e32 v75, v76
	v_add_f32_e32 v179, v74, v90
	v_exp_f32_e32 v92, v93
	v_mov_b32_e32 v76, v77
	v_add_f32_e32 v77, v179, v178
	v_add_f32_e32 v93, v75, v91
	v_add_f32_e32 v178, v93, v77
	v_exp_f32_e32 v76, v76
	v_exp_f32_e32 v93, v94
	v_exp_f32_e32 v77, v78
	v_add_f32_e32 v179, v76, v92
	v_exp_f32_e32 v94, v95
	v_mov_b32_e32 v78, v79
	v_add_f32_e32 v79, v179, v178
	v_add_f32_e32 v95, v77, v93
	v_exp_f32_e32 v78, v78
	v_add_f32_e32 v79, v95, v79
	v_exp_f32_e32 v95, v96
	v_exp_f32_e32 v80, v80
	v_exp_f32_e32 v96, v97
	v_exp_f32_e32 v81, v81
	v_add_f32_e32 v178, v78, v94
	v_add_f32_e32 v79, v178, v79
	v_add_f32_e32 v97, v80, v95
	v_add_f32_e32 v79, v97, v79
	v_add_f32_e32 v97, v81, v96
	v_add_f32_e32 v79, v97, v79
	v_cmp_ge_f32_e32 vcc, 0x453504f3, v79
	s_cmp_eq_u64 vcc, exec
	s_cbranch_scc0 .Lsm1_slow
	v_mov_b32_e32 v97, 1.0
	s_branch .LBB0_813


.Lsm1_join:
	s_cbranch_vccz .LBB0_813
	s_and_saveexec_b64 s[56:57], s[0:1]
	ds_write_b32 v160, v97
	s_or_b64 exec, exec, s[56:57]
	s_waitcnt lgkmcnt(0)
	v_add_u32_e32 v190, s65, v148
	ds_read_b128 v[178:181], v190 offset:96
	ds_read_b128 v[182:185], v190 offset:64
	ds_read_b128 v[186:189], v190 offset:32
	ds_read_b128 v[190:193], v190
	s_waitcnt lgkmcnt(0)
	v_pk_mul_f32 v[62:63], v[62:63], v[178:179]
	v_pk_mul_f32 v[58:59], v[58:59], v[182:183]
	v_pk_mul_f32 v[54:55], v[54:55], v[186:187]
	v_pk_mul_f32 v[64:65], v[64:65], v[180:181]
	v_pk_mul_f32 v[60:61], v[60:61], v[184:185]
	v_pk_mul_f32 v[56:57], v[56:57], v[188:189]
	v_pk_mul_f32 v[52:53], v[52:53], v[192:193]
	v_pk_mul_f32 v[50:51], v[50:51], v[190:191]
	v_pk_mul_f32 v[46:47], v[46:47], v[178:179]
	v_pk_mul_f32 v[42:43], v[42:43], v[182:183]
	v_pk_mul_f32 v[38:39], v[38:39], v[186:187]
	v_pk_mul_f32 v[48:49], v[48:49], v[180:181]
	v_pk_mul_f32 v[44:45], v[44:45], v[184:185]
	v_pk_mul_f32 v[40:41], v[40:41], v[188:189]
	v_pk_mul_f32 v[36:37], v[36:37], v[192:193]
	v_pk_mul_f32 v[34:35], v[34:35], v[190:191]
	v_pk_mul_f32 v[30:31], v[30:31], v[178:179]
	v_pk_mul_f32 v[26:27], v[26:27], v[182:183]
	v_pk_mul_f32 v[22:23], v[22:23], v[186:187]
	v_pk_mul_f32 v[32:33], v[32:33], v[180:181]
	v_pk_mul_f32 v[28:29], v[28:29], v[184:185]
	v_pk_mul_f32 v[24:25], v[24:25], v[188:189]
	v_pk_mul_f32 v[20:21], v[20:21], v[192:193]
	v_pk_mul_f32 v[18:19], v[18:19], v[190:191]
	v_pk_mul_f32 v[14:15], v[14:15], v[178:179]
	v_pk_mul_f32 v[10:11], v[10:11], v[182:183]
	v_pk_mul_f32 v[6:7], v[6:7], v[186:187]
	v_pk_mul_f32 v[16:17], v[16:17], v[180:181]
	v_pk_mul_f32 v[12:13], v[12:13], v[184:185]
	v_pk_mul_f32 v[8:9], v[8:9], v[188:189]
	v_pk_mul_f32 v[4:5], v[4:5], v[192:193]
	v_pk_mul_f32 v[2:3], v[2:3], v[190:191]

.Lsm1_slow:
	s_mul_i32 s56, s87, 0x6000
	s_add_i32 s56, s56, 0
	s_add_i32 s56, s56, 0x8000
	v_add_u32_e32 v175, s56, v161
	ds_read_b128 v[66:69], v175 offset:0
	ds_read_b128 v[70:73], v175 offset:0x3000
	v_add_u32_e32 v200, s56, v169
	ds_read_b128 v[176:179], v200 offset:0
	ds_read_b128 v[180:183], v200 offset:0x3000
	v_add_u32_e32 v201, s56, v170
	ds_read_b128 v[184:187], v201 offset:0
	ds_read_b128 v[188:191], v201 offset:0x3000
	s_waitcnt lgkmcnt(4)
	v_add_u32_e32 v202, s56, v171
	v_mfma_f32_32x32x16_bf16 v[82:97], v[66:69], v[98:101], v[206:221]
	ds_read_b128 v[192:195], v202 offset:0
	ds_read_b128 v[196:199], v202 offset:0x3000
	s_waitcnt lgkmcnt(4)
	v_mfma_f32_32x32x16_bf16 v[66:81], v[70:73], v[98:101], v[206:221]
	v_mfma_f32_32x32x16_bf16 v[82:97], v[176:179], v[102:105], v[82:97]
	ds_read_b128 v[176:179], v175 offset:0x80
	v_mfma_f32_32x32x16_bf16 v[66:81], v[180:183], v[102:105], v[66:81]
	ds_read_b128 v[180:183], v175 offset:0x3080
	s_waitcnt lgkmcnt(4)
	v_mfma_f32_32x32x16_bf16 v[82:97], v[184:187], v[106:109], v[82:97]
	ds_read_b128 v[184:187], v200 offset:0x80
	v_mfma_f32_32x32x16_bf16 v[66:81], v[188:191], v[106:109], v[66:81]
	ds_read_b128 v[188:191], v200 offset:0x3080
	s_waitcnt lgkmcnt(4)
	v_mfma_f32_32x32x16_bf16 v[82:97], v[192:195], v[110:113], v[82:97]
	ds_read_b128 v[192:195], v201 offset:0x80
	v_mfma_f32_32x32x16_bf16 v[66:81], v[196:199], v[110:113], v[66:81]
	ds_read_b128 v[196:199], v201 offset:0x3080
	s_waitcnt lgkmcnt(4)
	v_mfma_f32_32x32x16_bf16 v[82:97], v[176:179], v[114:117], v[82:97]
	ds_read_b128 v[176:179], v202 offset:0x80
	v_mfma_f32_32x32x16_bf16 v[66:81], v[180:183], v[114:117], v[66:81]
	ds_read_b128 v[180:183], v202 offset:0x3080
	s_waitcnt lgkmcnt(4)
	v_mfma_f32_32x32x16_bf16 v[82:97], v[184:187], v[118:121], v[82:97]
	ds_read_b128 v[184:187], v175 offset:0x100
	v_mfma_f32_32x32x16_bf16 v[66:81], v[188:191], v[118:121], v[66:81]
	ds_read_b128 v[188:191], v175 offset:0x3100
	s_waitcnt lgkmcnt(4)
	v_mfma_f32_32x32x16_bf16 v[82:97], v[192:195], v[122:125], v[82:97]
	ds_read_b128 v[192:195], v200 offset:0x100
	v_mfma_f32_32x32x16_bf16 v[66:81], v[196:199], v[122:125], v[66:81]
	ds_read_b128 v[196:199], v200 offset:0x3100
	s_waitcnt lgkmcnt(4)
	v_mfma_f32_32x32x16_bf16 v[82:97], v[176:179], v[126:129], v[82:97]
	ds_read_b128 v[176:179], v201 offset:0x100
	v_mfma_f32_32x32x16_bf16 v[66:81], v[180:183], v[126:129], v[66:81]
	ds_read_b128 v[180:183], v201 offset:0x3100
	s_waitcnt lgkmcnt(4)
	v_mfma_f32_32x32x16_bf16 v[82:97], v[184:187], v[130:133], v[82:97]
	ds_read_b128 v[184:187], v202 offset:0x100
	v_mfma_f32_32x32x16_bf16 v[66:81], v[188:191], v[130:133], v[66:81]
	ds_read_b128 v[188:191], v202 offset:0x3100
	s_waitcnt lgkmcnt(4)
	v_mfma_f32_32x32x16_bf16 v[82:97], v[192:195], v[134:137], v[82:97]
	s_waitcnt lgkmcnt(2)
	v_mfma_f32_32x32x16_bf16 v[66:81], v[196:199], v[134:137], v[66:81]
	v_mfma_f32_32x32x16_bf16 v[82:97], v[176:179], v[138:141], v[82:97]
	s_waitcnt lgkmcnt(0)
	v_mfma_f32_32x32x16_bf16 v[66:81], v[180:183], v[138:141], v[66:81]
	v_mfma_f32_32x32x16_bf16 v[82:97], v[184:187], v[142:145], v[82:97]
	v_mfma_f32_32x32x16_bf16 v[66:81], v[188:191], v[142:145], v[66:81]
	s_add_i32 s56, s86, 0x13f
	s_cmp_le_i32 s56, s84
	s_cbranch_scc1 .Lsm1_nomask
	v_add_u32_e32 v175, s83, v168
	v_cmp_lt_i32_e32 vcc, -1, v175
	v_add_u32_e32 v176, -1, v175
	s_nop 4
	v_cndmask_b32_e32 v82, v165, v82, vcc
	v_cmp_lt_i32_e32 vcc, 31, v175
	s_nop 1
	v_cndmask_b32_e32 v66, v165, v66, vcc
	v_cmp_lt_i32_e32 vcc, -1, v176
	s_nop 1
	v_cndmask_b32_e32 v83, v165, v83, vcc
	v_cmp_lt_i32_e32 vcc, 31, v176
	v_add_u32_e32 v176, -2, v175
	s_nop 0
	v_cndmask_b32_e32 v67, v165, v67, vcc
	v_cmp_lt_i32_e32 vcc, -1, v176
	s_nop 1
	v_cndmask_b32_e32 v84, v165, v84, vcc
	v_cmp_lt_i32_e32 vcc, 31, v176
	v_add_u32_e32 v176, -3, v175
	s_nop 0
	v_cndmask_b32_e32 v68, v165, v68, vcc
	v_cmp_lt_i32_e32 vcc, -1, v176
	s_nop 1
	v_cndmask_b32_e32 v85, v165, v85, vcc
	v_cmp_lt_i32_e32 vcc, 31, v176
	v_add_u32_e32 v176, -4, v175
	s_nop 0
	v_cndmask_b32_e32 v69, v165, v69, vcc
	v_cmp_lt_i32_e32 vcc, -1, v176
	s_nop 1
	v_cndmask_b32_e32 v86, v165, v86, vcc
	v_cmp_lt_i32_e32 vcc, 31, v176
	v_add_u32_e32 v176, -5, v175
	s_nop 0
	v_cndmask_b32_e32 v70, v165, v70, vcc
	v_cmp_lt_i32_e32 vcc, -1, v176
	s_nop 1
	v_cndmask_b32_e32 v87, v165, v87, vcc
	v_cmp_lt_i32_e32 vcc, 31, v176
	v_add_u32_e32 v176, -6, v175
	s_nop 0
	v_cndmask_b32_e32 v71, v165, v71, vcc
	v_cmp_lt_i32_e32 vcc, -1, v176
	s_nop 1
	v_cndmask_b32_e32 v88, v165, v88, vcc
	v_cmp_lt_i32_e32 vcc, 31, v176
	v_add_u32_e32 v176, -7, v175
	s_nop 0
	v_cndmask_b32_e32 v72, v165, v72, vcc
	v_cmp_lt_i32_e32 vcc, -1, v176
	s_nop 1
	v_cndmask_b32_e32 v89, v165, v89, vcc
	v_cmp_lt_i32_e32 vcc, 31, v176
	v_add_u32_e32 v176, -16, v175
	s_nop 0
	v_cndmask_b32_e32 v73, v165, v73, vcc
	v_cmp_lt_i32_e32 vcc, -1, v176
	s_nop 1
	v_cndmask_b32_e32 v90, v165, v90, vcc
	v_cmp_lt_i32_e32 vcc, 31, v176
	v_subrev_u32_e32 v176, 17, v175
	s_nop 0
	v_cndmask_b32_e32 v74, v165, v74, vcc
	v_cmp_lt_i32_e32 vcc, -1, v176
	s_nop 1
	v_cndmask_b32_e32 v91, v165, v91, vcc
	v_cmp_lt_i32_e32 vcc, 31, v176
	v_subrev_u32_e32 v176, 18, v175
	s_nop 0
	v_cndmask_b32_e32 v75, v165, v75, vcc
	v_cmp_lt_i32_e32 vcc, -1, v176
	s_nop 1
	v_cndmask_b32_e32 v92, v165, v92, vcc
	v_cmp_lt_i32_e32 vcc, 31, v176
	v_subrev_u32_e32 v176, 19, v175
	s_nop 0
	v_cndmask_b32_e32 v76, v165, v76, vcc
	v_cmp_lt_i32_e32 vcc, -1, v176
	s_nop 1
	v_cndmask_b32_e32 v93, v165, v93, vcc
	v_cmp_lt_i32_e32 vcc, 31, v176
	v_subrev_u32_e32 v176, 20, v175
	s_nop 0
	v_cndmask_b32_e32 v77, v165, v77, vcc
	v_cmp_lt_i32_e32 vcc, -1, v176
	s_nop 1
	v_cndmask_b32_e32 v94, v165, v94, vcc
	v_cmp_lt_i32_e32 vcc, 31, v176
	v_subrev_u32_e32 v176, 21, v175
	s_nop 0
	v_cndmask_b32_e32 v78, v165, v78, vcc
	v_cmp_lt_i32_e32 vcc, -1, v176
	s_nop 1
	v_cndmask_b32_e32 v95, v165, v95, vcc
	v_cmp_lt_i32_e32 vcc, 31, v176
	v_subrev_u32_e32 v176, 22, v175
	v_subrev_u32_e32 v175, 23, v175
	v_cndmask_b32_e32 v79, v165, v79, vcc
	v_cmp_lt_i32_e32 vcc, -1, v176
	s_nop 1
	v_cndmask_b32_e32 v96, v165, v96, vcc
	v_cmp_lt_i32_e32 vcc, 31, v176
	s_nop 1
	v_cndmask_b32_e32 v80, v165, v80, vcc
	v_cmp_lt_i32_e32 vcc, -1, v175
	s_nop 1
	v_cndmask_b32_e32 v97, v165, v97, vcc
	v_cmp_lt_i32_e32 vcc, 31, v175
	s_nop 1
	v_cndmask_b32_e32 v81, v165, v81, vcc
.Lsm1_nomask:
	s_nop 7
	v_max_f32_e32 v175, v82, v83


	v_max3_f32 v175, v175, v84, v85
	v_max3_f32 v175, v175, v86, v87
	v_max3_f32 v175, v175, v88, v89
	v_max3_f32 v175, v175, v90, v91
	v_max3_f32 v175, v175, v92, v93
	v_max3_f32 v175, v175, v94, v95
	v_max3_f32 v175, v175, v96, v97
	v_max3_f32 v175, v175, v66, v67
	v_max3_f32 v175, v175, v68, v69
	v_max3_f32 v175, v175, v70, v71
	v_max3_f32 v175, v175, v72, v73
	v_max3_f32 v175, v175, v74, v75
	v_max3_f32 v175, v175, v76, v77
	v_max3_f32 v175, v175, v78, v79
	v_max3_f32 v175, v175, v80, v81
	v_mov_b32_e32 v176, v175
	s_nop 1
	v_permlane32_swap_b32_e32 v175, v176
	v_max_f32_e32 v175, v175, v176
	v_max_f32_e32 v175, 0, v175
	v_sub_f32_e32 v66, v66, v175
	v_sub_f32_e32 v67, v67, v175
	v_sub_f32_e32 v68, v68, v175
	v_sub_f32_e32 v69, v69, v175
	v_sub_f32_e32 v70, v70, v175
	v_sub_f32_e32 v71, v71, v175
	v_sub_f32_e32 v72, v72, v175
	v_sub_f32_e32 v73, v73, v175
	v_sub_f32_e32 v74, v74, v175
	v_sub_f32_e32 v75, v75, v175
	v_sub_f32_e32 v76, v76, v175
	v_sub_f32_e32 v77, v77, v175
	v_sub_f32_e32 v78, v78, v175
	v_sub_f32_e32 v79, v79, v175
	v_sub_f32_e32 v80, v80, v175
	v_sub_f32_e32 v81, v81, v175
	v_sub_f32_e32 v82, v82, v175
	v_sub_f32_e32 v83, v83, v175
	v_sub_f32_e32 v84, v84, v175
	v_sub_f32_e32 v85, v85, v175
	v_sub_f32_e32 v86, v86, v175
	v_sub_f32_e32 v87, v87, v175
	v_sub_f32_e32 v88, v88, v175
	v_sub_f32_e32 v89, v89, v175
	v_sub_f32_e32 v90, v90, v175
	v_sub_f32_e32 v91, v91, v175
	v_sub_f32_e32 v92, v92, v175
	v_sub_f32_e32 v93, v93, v175
	v_sub_f32_e32 v94, v94, v175
	v_sub_f32_e32 v95, v95, v175
	v_sub_f32_e32 v96, v96, v175
	v_sub_f32_e32 v97, v97, v175
	v_exp_f32_e64 v222, -v175
	v_add_f32_e32 v173, v173, v175
	v_sub_f32_e32 v206, 0, v173
	v_mov_b32_e32 v207, v206
	v_mov_b32_e32 v208, v206
	v_mov_b32_e32 v209, v206
	v_mov_b32_e32 v210, v206
	v_mov_b32_e32 v211, v206
	v_mov_b32_e32 v212, v206
	v_mov_b32_e32 v213, v206
	v_mov_b32_e32 v214, v206
	v_mov_b32_e32 v215, v206
	v_mov_b32_e32 v216, v206
	v_mov_b32_e32 v217, v206
	v_mov_b32_e32 v218, v206
	v_mov_b32_e32 v219, v206
	v_mov_b32_e32 v220, v206
	v_mov_b32_e32 v221, v206
	v_exp_f32_e32 v82, v82
	v_exp_f32_e32 v66, v66
	v_exp_f32_e32 v175, v83
	v_exp_f32_e32 v67, v67
	v_exp_f32_e32 v84, v84
	v_exp_f32_e32 v68, v68
	v_exp_f32_e32 v85, v85
	v_exp_f32_e32 v69, v69
	v_add_f32_e32 v83, v66, v82
	v_exp_f32_e32 v86, v86
	v_exp_f32_e32 v70, v70
	v_add_f32_e32 v83, 0, v83
	v_add_f32_e32 v176, v67, v175
	v_add_f32_e32 v83, v176, v83
	v_add_f32_e32 v176, v68, v84
	v_add_f32_e32 v83, v176, v83
	v_add_f32_e32 v176, v69, v85
	v_add_f32_e32 v83, v176, v83
	v_add_f32_e32 v176, v70, v86
	v_exp_f32_e32 v87, v87
	v_exp_f32_e32 v71, v71
	v_add_f32_e32 v178, v176, v83
	v_exp_f32_e32 v88, v88
	v_exp_f32_e32 v72, v72
	v_add_f32_e32 v179, v71, v87
	v_exp_f32_e32 v176, v89
	v_exp_f32_e32 v83, v73
	v_add_f32_e32 v73, v179, v178
	v_add_f32_e32 v89, v72, v88
	v_add_f32_e32 v178, v89, v73
	v_exp_f32_e32 v89, v90
	v_exp_f32_e32 v73, v74
	v_add_f32_e32 v179, v83, v176
	v_exp_f32_e32 v90, v91
	v_mov_b32_e32 v74, v75
	v_add_f32_e32 v75, v179, v178
	v_add_f32_e32 v91, v73, v89
	v_add_f32_e32 v178, v91, v75
	v_exp_f32_e32 v74, v74
	v_exp_f32_e32 v91, v92
	v_exp_f32_e32 v75, v76
	v_add_f32_e32 v179, v74, v90
	v_exp_f32_e32 v92, v93
	v_mov_b32_e32 v76, v77
	v_add_f32_e32 v77, v179, v178
	v_add_f32_e32 v93, v75, v91
	v_add_f32_e32 v178, v93, v77
	v_exp_f32_e32 v76, v76
	v_exp_f32_e32 v93, v94
	v_exp_f32_e32 v77, v78
	v_add_f32_e32 v179, v76, v92
	v_exp_f32_e32 v94, v95
	v_mov_b32_e32 v78, v79
	v_add_f32_e32 v79, v179, v178
	v_add_f32_e32 v95, v77, v93
	v_exp_f32_e32 v78, v78
	v_add_f32_e32 v79, v95, v79
	v_exp_f32_e32 v95, v96
	v_exp_f32_e32 v80, v80
	v_exp_f32_e32 v96, v97
	v_exp_f32_e32 v81, v81
	v_add_f32_e32 v178, v78, v94
	v_add_f32_e32 v79, v178, v79
	v_add_f32_e32 v97, v80, v95
	v_add_f32_e32 v79, v97, v79
	v_add_f32_e32 v97, v81, v96
	v_add_f32_e32 v79, v97, v79
	v_mov_b32_e32 v97, v222
	v_cmp_gt_f32_e32 vcc, 1.0, v97
	s_branch .Lsm1_join

.LBB0_950:
	s_nop 9
	v_exp_f32_e32 v177, v66
	v_exp_f32_e32 v66, v82
	v_exp_f32_e32 v178, v67
	v_exp_f32_e32 v67, v83
	v_exp_f32_e32 v83, v68
	v_exp_f32_e32 v68, v84
	v_add_f32_e32 v82, v66, v177
	v_add_f32_e32 v82, 0, v82
	v_add_f32_e32 v179, v67, v178
	v_exp_f32_e32 v84, v69
	v_add_f32_e32 v82, v179, v82
	v_mov_b32_e32 v69, v85
	v_add_f32_e32 v85, v68, v83
	v_exp_f32_e32 v69, v69
	v_add_f32_e32 v82, v85, v82
	v_exp_f32_e32 v85, v70
	v_exp_f32_e32 v70, v86
	v_add_f32_e32 v179, v69, v84
	v_exp_f32_e32 v86, v71
	v_add_f32_e32 v82, v179, v82
	v_mov_b32_e32 v71, v87
	v_add_f32_e32 v87, v70, v85
	v_exp_f32_e32 v71, v71
	v_add_f32_e32 v181, v87, v82
	v_exp_f32_e32 v87, v72
	v_exp_f32_e32 v72, v88
	v_add_f32_e32 v182, v71, v86
	v_exp_f32_e32 v179, v73
	v_exp_f32_e32 v82, v89
	v_add_f32_e32 v73, v182, v181
	v_add_f32_e32 v88, v72, v87
	v_add_f32_e32 v181, v88, v73
	v_exp_f32_e32 v88, v74
	v_exp_f32_e32 v73, v90
	v_add_f32_e32 v182, v82, v179
	v_mov_b32_e32 v74, v75
	v_add_f32_e32 v75, v182, v181
	v_add_f32_e32 v90, v73, v88
	v_exp_f32_e32 v89, v74
	v_add_f32_e32 v181, v90, v75
	v_exp_f32_e32 v74, v91
	v_exp_f32_e32 v90, v76
	v_exp_f32_e32 v75, v92
	v_add_f32_e32 v182, v74, v89
	v_mov_b32_e32 v76, v77
	v_add_f32_e32 v77, v182, v181
	v_add_f32_e32 v92, v75, v90
	v_exp_f32_e32 v91, v76
	v_add_f32_e32 v181, v92, v77
	v_exp_f32_e32 v76, v93
	v_exp_f32_e32 v92, v78
	v_exp_f32_e32 v77, v94
	v_add_f32_e32 v182, v76, v91
	v_mov_b32_e32 v78, v79
	v_add_f32_e32 v79, v182, v181
	v_add_f32_e32 v94, v77, v92
	v_exp_f32_e32 v93, v78
	v_add_f32_e32 v181, v94, v79
	v_exp_f32_e32 v78, v95
	v_exp_f32_e32 v94, v80
	v_exp_f32_e32 v79, v96
	v_exp_f32_e32 v95, v81
	v_exp_f32_e32 v80, v97
	v_add_f32_e32 v182, v78, v93
	v_add_f32_e32 v81, v182, v181
	v_add_f32_e32 v96, v79, v94
	v_add_f32_e32 v81, v96, v81
	v_add_f32_e32 v96, v80, v95
	v_add_f32_e32 v81, v96, v81
	v_cmp_ge_f32_e32 vcc, 0x453504f3, v81
	s_cmp_eq_u64 vcc, exec
	s_cbranch_scc0 .Lsm2_slow
	v_mov_b32_e32 v96, 1.0
	s_branch .LBB0_954


.Lsm2_join:
	s_cbranch_vccz .LBB0_954
	s_and_saveexec_b64 s[44:45], s[0:1]
	ds_write_b32 v168, v96
	s_or_b64 exec, exec, s[44:45]
	s_waitcnt lgkmcnt(0)
	v_add_u32_e32 v192, s65, v148
	ds_read_b128 v[180:183], v192 offset:96
	ds_read_b128 v[184:187], v192 offset:64
	ds_read_b128 v[188:191], v192 offset:32
	ds_read_b128 v[192:195], v192
	s_waitcnt lgkmcnt(0)
	v_pk_mul_f32 v[62:63], v[62:63], v[180:181]
	v_pk_mul_f32 v[58:59], v[58:59], v[184:185]
	v_pk_mul_f32 v[54:55], v[54:55], v[188:189]
	v_pk_mul_f32 v[64:65], v[64:65], v[182:183]
	v_pk_mul_f32 v[60:61], v[60:61], v[186:187]
	v_pk_mul_f32 v[56:57], v[56:57], v[190:191]
	v_pk_mul_f32 v[52:53], v[52:53], v[194:195]
	v_pk_mul_f32 v[50:51], v[50:51], v[192:193]
	v_pk_mul_f32 v[46:47], v[46:47], v[180:181]
	v_pk_mul_f32 v[42:43], v[42:43], v[184:185]
	v_pk_mul_f32 v[38:39], v[38:39], v[188:189]
	v_pk_mul_f32 v[48:49], v[48:49], v[182:183]
	v_pk_mul_f32 v[44:45], v[44:45], v[186:187]
	v_pk_mul_f32 v[40:41], v[40:41], v[190:191]
	v_pk_mul_f32 v[36:37], v[36:37], v[194:195]
	v_pk_mul_f32 v[34:35], v[34:35], v[192:193]
	v_pk_mul_f32 v[30:31], v[30:31], v[180:181]
	v_pk_mul_f32 v[26:27], v[26:27], v[184:185]
	v_pk_mul_f32 v[22:23], v[22:23], v[188:189]
	v_pk_mul_f32 v[32:33], v[32:33], v[182:183]
	v_pk_mul_f32 v[28:29], v[28:29], v[186:187]
	v_pk_mul_f32 v[24:25], v[24:25], v[190:191]
	v_pk_mul_f32 v[20:21], v[20:21], v[194:195]
	v_pk_mul_f32 v[18:19], v[18:19], v[192:193]
	v_pk_mul_f32 v[14:15], v[14:15], v[180:181]
	v_pk_mul_f32 v[10:11], v[10:11], v[184:185]
	v_pk_mul_f32 v[6:7], v[6:7], v[188:189]
	v_pk_mul_f32 v[16:17], v[16:17], v[182:183]
	v_pk_mul_f32 v[12:13], v[12:13], v[186:187]
	v_pk_mul_f32 v[8:9], v[8:9], v[190:191]
	v_pk_mul_f32 v[4:5], v[4:5], v[194:195]
	v_pk_mul_f32 v[2:3], v[2:3], v[192:193]

.Lsm2_slow:
	s_mul_i32 s44, s48, 0x6000
	s_add_i32 s44, s44, 0
	s_add_i32 s44, s44, 0x8000
	v_add_u32_e32 v177, s44, v171
	ds_read_b128 v[66:69], v177 offset:0
	ds_read_b128 v[82:85], v177 offset:0x3000
	v_add_u32_e32 v206, s44, v172
	ds_read_b128 v[178:181], v206 offset:0
	ds_read_b128 v[182:185], v206 offset:0x3000
	v_add_u32_e32 v207, s44, v173
	ds_read_b128 v[186:189], v207 offset:0
	ds_read_b128 v[190:193], v207 offset:0x3000
	s_waitcnt lgkmcnt(4)
	v_add_u32_e32 v208, s44, v174
	v_mfma_f32_32x32x16_bf16 v[66:81], v[66:69], v[98:101], v[210:225]
	ds_read_b128 v[194:197], v208 offset:0
	ds_read_b128 v[198:201], v208 offset:0x3000
	s_waitcnt lgkmcnt(4)
	v_mfma_f32_32x32x16_bf16 v[82:97], v[82:85], v[98:101], v[210:225]
	v_mfma_f32_32x32x16_bf16 v[66:81], v[178:181], v[102:105], v[66:81]
	ds_read_b128 v[178:181], v177 offset:0x80
	ds_read_b128 v[202:205], v177 offset:0x3080
	s_waitcnt lgkmcnt(4)
	v_mfma_f32_32x32x16_bf16 v[82:97], v[182:185], v[102:105], v[82:97]
	v_mfma_f32_32x32x16_bf16 v[66:81], v[186:189], v[106:109], v[66:81]
	ds_read_b128 v[182:185], v206 offset:0x80
	ds_read_b128 v[186:189], v206 offset:0x3080
	s_waitcnt lgkmcnt(4)
	v_mfma_f32_32x32x16_bf16 v[82:97], v[190:193], v[106:109], v[82:97]
	v_mfma_f32_32x32x16_bf16 v[66:81], v[194:197], v[110:113], v[66:81]
	ds_read_b128 v[190:193], v207 offset:0x80
	ds_read_b128 v[194:197], v207 offset:0x3080
	s_waitcnt lgkmcnt(4)
	v_mfma_f32_32x32x16_bf16 v[82:97], v[198:201], v[110:113], v[82:97]
	v_mfma_f32_32x32x16_bf16 v[66:81], v[178:181], v[114:117], v[66:81]
	ds_read_b128 v[178:181], v208 offset:0x80
	ds_read_b128 v[198:201], v208 offset:0x3080
	s_waitcnt lgkmcnt(4)
	v_mfma_f32_32x32x16_bf16 v[82:97], v[202:205], v[114:117], v[82:97]
	v_mfma_f32_32x32x16_bf16 v[66:81], v[182:185], v[118:121], v[66:81]
	ds_read_b128 v[182:185], v177 offset:0x100
	ds_read_b128 v[202:205], v177 offset:0x3100
	s_waitcnt lgkmcnt(4)
	v_mfma_f32_32x32x16_bf16 v[82:97], v[186:189], v[118:121], v[82:97]
	v_mfma_f32_32x32x16_bf16 v[66:81], v[190:193], v[122:125], v[66:81]
	ds_read_b128 v[186:189], v206 offset:0x100
	ds_read_b128 v[190:193], v206 offset:0x3100
	s_waitcnt lgkmcnt(4)
	v_mfma_f32_32x32x16_bf16 v[82:97], v[194:197], v[122:125], v[82:97]
	v_mfma_f32_32x32x16_bf16 v[66:81], v[178:181], v[126:129], v[66:81]
	ds_read_b128 v[178:181], v207 offset:0x100
	ds_read_b128 v[194:197], v207 offset:0x3100
	s_waitcnt lgkmcnt(4)
	v_mfma_f32_32x32x16_bf16 v[82:97], v[198:201], v[126:129], v[82:97]
	v_mfma_f32_32x32x16_bf16 v[66:81], v[182:185], v[130:133], v[66:81]
	ds_read_b128 v[182:185], v208 offset:0x100
	ds_read_b128 v[198:201], v208 offset:0x3100
	s_waitcnt lgkmcnt(4)
	v_mfma_f32_32x32x16_bf16 v[82:97], v[202:205], v[130:133], v[82:97]
	v_mfma_f32_32x32x16_bf16 v[66:81], v[186:189], v[134:137], v[66:81]
	s_waitcnt lgkmcnt(2)
	v_mfma_f32_32x32x16_bf16 v[82:97], v[190:193], v[134:137], v[82:97]
	v_mfma_f32_32x32x16_bf16 v[66:81], v[178:181], v[138:141], v[66:81]
	s_waitcnt lgkmcnt(0)
	v_mfma_f32_32x32x16_bf16 v[82:97], v[194:197], v[138:141], v[82:97]
	v_mfma_f32_32x32x16_bf16 v[66:81], v[182:185], v[142:145], v[66:81]
	v_mfma_f32_32x32x16_bf16 v[82:97], v[198:201], v[142:145], v[82:97]
	s_add_i32 s44, s47, 0x13f
	s_cmp_le_i32 s44, s55
	s_cbranch_scc1 .Lsm2_nomask
	v_add_u32_e32 v177, s54, v167
	v_cmp_lt_i32_e32 vcc, -1, v177
	v_add_u32_e32 v178, -1, v177
	s_nop 4
	v_cndmask_b32_e32 v66, v165, v66, vcc
	v_cmp_lt_i32_e32 vcc, 31, v177
	s_nop 1
	v_cndmask_b32_e32 v82, v165, v82, vcc
	v_cmp_lt_i32_e32 vcc, -1, v178
	s_nop 1
	v_cndmask_b32_e32 v67, v165, v67, vcc
	v_cmp_lt_i32_e32 vcc, 31, v178
	v_add_u32_e32 v178, -2, v177
	s_nop 0
	v_cndmask_b32_e32 v83, v165, v83, vcc
	v_cmp_lt_i32_e32 vcc, -1, v178
	s_nop 1
	v_cndmask_b32_e32 v68, v165, v68, vcc
	v_cmp_lt_i32_e32 vcc, 31, v178
	v_add_u32_e32 v178, -3, v177
	s_nop 0
	v_cndmask_b32_e32 v84, v165, v84, vcc
	v_cmp_lt_i32_e32 vcc, -1, v178
	s_nop 1
	v_cndmask_b32_e32 v69, v165, v69, vcc
	v_cmp_lt_i32_e32 vcc, 31, v178
	v_add_u32_e32 v178, -4, v177
	s_nop 0
	v_cndmask_b32_e32 v85, v165, v85, vcc
	v_cmp_lt_i32_e32 vcc, -1, v178
	s_nop 1
	v_cndmask_b32_e32 v70, v165, v70, vcc
	v_cmp_lt_i32_e32 vcc, 31, v178
	v_add_u32_e32 v178, -5, v177
	s_nop 0
	v_cndmask_b32_e32 v86, v165, v86, vcc
	v_cmp_lt_i32_e32 vcc, -1, v178
	s_nop 1
	v_cndmask_b32_e32 v71, v165, v71, vcc
	v_cmp_lt_i32_e32 vcc, 31, v178
	v_add_u32_e32 v178, -6, v177
	s_nop 0
	v_cndmask_b32_e32 v87, v165, v87, vcc
	v_cmp_lt_i32_e32 vcc, -1, v178
	s_nop 1
	v_cndmask_b32_e32 v72, v165, v72, vcc
	v_cmp_lt_i32_e32 vcc, 31, v178
	v_add_u32_e32 v178, -7, v177
	s_nop 0
	v_cndmask_b32_e32 v88, v165, v88, vcc
	v_cmp_lt_i32_e32 vcc, -1, v178
	s_nop 1
	v_cndmask_b32_e32 v73, v165, v73, vcc
	v_cmp_lt_i32_e32 vcc, 31, v178
	v_add_u32_e32 v178, -16, v177
	s_nop 0
	v_cndmask_b32_e32 v89, v165, v89, vcc
	v_cmp_lt_i32_e32 vcc, -1, v178
	s_nop 1
	v_cndmask_b32_e32 v74, v165, v74, vcc
	v_cmp_lt_i32_e32 vcc, 31, v178
	v_subrev_u32_e32 v178, 17, v177
	s_nop 0
	v_cndmask_b32_e32 v90, v165, v90, vcc
	v_cmp_lt_i32_e32 vcc, -1, v178
	s_nop 1
	v_cndmask_b32_e32 v75, v165, v75, vcc
	v_cmp_lt_i32_e32 vcc, 31, v178
	v_subrev_u32_e32 v178, 18, v177
	s_nop 0
	v_cndmask_b32_e32 v91, v165, v91, vcc
	v_cmp_lt_i32_e32 vcc, -1, v178
	s_nop 1
	v_cndmask_b32_e32 v76, v165, v76, vcc
	v_cmp_lt_i32_e32 vcc, 31, v178
	v_subrev_u32_e32 v178, 19, v177
	s_nop 0
	v_cndmask_b32_e32 v92, v165, v92, vcc
	v_cmp_lt_i32_e32 vcc, -1, v178
	s_nop 1
	v_cndmask_b32_e32 v77, v165, v77, vcc
	v_cmp_lt_i32_e32 vcc, 31, v178
	v_subrev_u32_e32 v178, 20, v177
	s_nop 0
	v_cndmask_b32_e32 v93, v165, v93, vcc
	v_cmp_lt_i32_e32 vcc, -1, v178
	s_nop 1
	v_cndmask_b32_e32 v78, v165, v78, vcc
	v_cmp_lt_i32_e32 vcc, 31, v178
	v_subrev_u32_e32 v178, 21, v177
	s_nop 0
	v_cndmask_b32_e32 v94, v165, v94, vcc
	v_cmp_lt_i32_e32 vcc, -1, v178
	s_nop 1
	v_cndmask_b32_e32 v79, v165, v79, vcc
	v_cmp_lt_i32_e32 vcc, 31, v178
	v_subrev_u32_e32 v178, 22, v177
	v_subrev_u32_e32 v177, 23, v177
	v_cndmask_b32_e32 v95, v165, v95, vcc
	v_cmp_lt_i32_e32 vcc, -1, v178
	s_nop 1
	v_cndmask_b32_e32 v80, v165, v80, vcc
	v_cmp_lt_i32_e32 vcc, 31, v178
	s_nop 1
	v_cndmask_b32_e32 v96, v165, v96, vcc
	v_cmp_lt_i32_e32 vcc, -1, v177
	s_nop 1
	v_cndmask_b32_e32 v81, v165, v81, vcc
	v_cmp_lt_i32_e32 vcc, 31, v177
	s_nop 1
	v_cndmask_b32_e32 v97, v165, v97, vcc
.Lsm2_nomask:
	s_nop 7
	v_max_f32_e32 v177, v66, v67


	v_max3_f32 v177, v177, v68, v69
	v_max3_f32 v177, v177, v70, v71
	v_max3_f32 v177, v177, v72, v73
	v_max3_f32 v177, v177, v74, v75
	v_max3_f32 v177, v177, v76, v77
	v_max3_f32 v177, v177, v78, v79
	v_max3_f32 v177, v177, v80, v81
	v_max3_f32 v177, v177, v82, v83
	v_max3_f32 v177, v177, v84, v85
	v_max3_f32 v177, v177, v86, v87
	v_max3_f32 v177, v177, v88, v89
	v_max3_f32 v177, v177, v90, v91
	v_max3_f32 v177, v177, v92, v93
	v_max3_f32 v177, v177, v94, v95
	v_max3_f32 v177, v177, v96, v97
	v_mov_b32_e32 v178, v177
	s_nop 1
	v_permlane32_swap_b32_e32 v177, v178
	v_max_f32_e32 v177, v177, v178
	v_max_f32_e32 v177, 0, v177
	v_sub_f32_e32 v66, v66, v177
	v_sub_f32_e32 v67, v67, v177
	v_sub_f32_e32 v68, v68, v177
	v_sub_f32_e32 v69, v69, v177
	v_sub_f32_e32 v70, v70, v177
	v_sub_f32_e32 v71, v71, v177
	v_sub_f32_e32 v72, v72, v177
	v_sub_f32_e32 v73, v73, v177
	v_sub_f32_e32 v74, v74, v177
	v_sub_f32_e32 v75, v75, v177
	v_sub_f32_e32 v76, v76, v177
	v_sub_f32_e32 v77, v77, v177
	v_sub_f32_e32 v78, v78, v177
	v_sub_f32_e32 v79, v79, v177
	v_sub_f32_e32 v80, v80, v177
	v_sub_f32_e32 v81, v81, v177
	v_sub_f32_e32 v82, v82, v177
	v_sub_f32_e32 v83, v83, v177
	v_sub_f32_e32 v84, v84, v177
	v_sub_f32_e32 v85, v85, v177
	v_sub_f32_e32 v86, v86, v177
	v_sub_f32_e32 v87, v87, v177
	v_sub_f32_e32 v88, v88, v177
	v_sub_f32_e32 v89, v89, v177
	v_sub_f32_e32 v90, v90, v177
	v_sub_f32_e32 v91, v91, v177
	v_sub_f32_e32 v92, v92, v177
	v_sub_f32_e32 v93, v93, v177
	v_sub_f32_e32 v94, v94, v177
	v_sub_f32_e32 v95, v95, v177
	v_sub_f32_e32 v96, v96, v177
	v_sub_f32_e32 v97, v97, v177
	v_exp_f32_e64 v226, -v177
	v_add_f32_e32 v175, v175, v177
	v_sub_f32_e32 v210, 0, v175
	v_mov_b32_e32 v211, v210
	v_mov_b32_e32 v212, v210
	v_mov_b32_e32 v213, v210
	v_mov_b32_e32 v214, v210
	v_mov_b32_e32 v215, v210
	v_mov_b32_e32 v216, v210
	v_mov_b32_e32 v217, v210
	v_mov_b32_e32 v218, v210
	v_mov_b32_e32 v219, v210
	v_mov_b32_e32 v220, v210
	v_mov_b32_e32 v221, v210
	v_mov_b32_e32 v222, v210
	v_mov_b32_e32 v223, v210
	v_mov_b32_e32 v224, v210
	v_mov_b32_e32 v225, v210
	v_exp_f32_e32 v177, v66
	v_exp_f32_e32 v66, v82
	v_exp_f32_e32 v178, v67
	v_exp_f32_e32 v67, v83
	v_exp_f32_e32 v83, v68
	v_exp_f32_e32 v68, v84
	v_add_f32_e32 v82, v66, v177
	v_add_f32_e32 v82, 0, v82
	v_add_f32_e32 v179, v67, v178
	v_exp_f32_e32 v84, v69
	v_add_f32_e32 v82, v179, v82
	v_mov_b32_e32 v69, v85
	v_add_f32_e32 v85, v68, v83
	v_exp_f32_e32 v69, v69
	v_add_f32_e32 v82, v85, v82
	v_exp_f32_e32 v85, v70
	v_exp_f32_e32 v70, v86
	v_add_f32_e32 v179, v69, v84
	v_exp_f32_e32 v86, v71
	v_add_f32_e32 v82, v179, v82
	v_mov_b32_e32 v71, v87
	v_add_f32_e32 v87, v70, v85
	v_exp_f32_e32 v71, v71
	v_add_f32_e32 v181, v87, v82
	v_exp_f32_e32 v87, v72
	v_exp_f32_e32 v72, v88
	v_add_f32_e32 v182, v71, v86
	v_exp_f32_e32 v179, v73
	v_exp_f32_e32 v82, v89
	v_add_f32_e32 v73, v182, v181
	v_add_f32_e32 v88, v72, v87
	v_add_f32_e32 v181, v88, v73
	v_exp_f32_e32 v88, v74
	v_exp_f32_e32 v73, v90
	v_add_f32_e32 v182, v82, v179
	v_mov_b32_e32 v74, v75
	v_add_f32_e32 v75, v182, v181
	v_add_f32_e32 v90, v73, v88
	v_exp_f32_e32 v89, v74
	v_add_f32_e32 v181, v90, v75
	v_exp_f32_e32 v74, v91
	v_exp_f32_e32 v90, v76
	v_exp_f32_e32 v75, v92
	v_add_f32_e32 v182, v74, v89
	v_mov_b32_e32 v76, v77
	v_add_f32_e32 v77, v182, v181
	v_add_f32_e32 v92, v75, v90
	v_exp_f32_e32 v91, v76
	v_add_f32_e32 v181, v92, v77
	v_exp_f32_e32 v76, v93
	v_exp_f32_e32 v92, v78
	v_exp_f32_e32 v77, v94
	v_add_f32_e32 v182, v76, v91
	v_mov_b32_e32 v78, v79
	v_add_f32_e32 v79, v182, v181
	v_add_f32_e32 v94, v77, v92
	v_exp_f32_e32 v93, v78
	v_add_f32_e32 v181, v94, v79
	v_exp_f32_e32 v78, v95
	v_exp_f32_e32 v94, v80
	v_exp_f32_e32 v79, v96
	v_exp_f32_e32 v95, v81
	v_exp_f32_e32 v80, v97
	v_add_f32_e32 v182, v78, v93
	v_add_f32_e32 v81, v182, v181
	v_add_f32_e32 v96, v79, v94
	v_add_f32_e32 v81, v96, v81
	v_add_f32_e32 v96, v80, v95
	v_add_f32_e32 v81, v96, v81
	v_mov_b32_e32 v96, v226
	v_cmp_gt_f32_e32 vcc, 1.0, v96
	s_branch .Lsm2_join
